# s16p + phase-0 gate-column/router gathers issued before the tile loop + attention lambda-parameter loads issued at the phase head (L0 and L1); padded incl. phase 0
# baseline (speedup 1.0000x reference)
; #define LAS __attribute__((address_space(3)))
; template <int PART> DI void prologue_phase(const Params& P, const Frame& F) {
;     LAS unsigned char* scr = F.lds + F.wave * 9216;
;     const int gw = (PART == 0 ? F.bid : F.bid - (GRID - NCONV)) * NWAVES + F.wave, NGW = (PART == 0 ? GRID : NCONV) * NWAVES;
;     constexpr int I_WIN = 32 * 112, I_WOUT = 32 * 32, I_GU = 32 * 224, I_DN = 112 * 32, I_PG = 32 * 32, I_PP = 4 * 32;
;     constexpr int C0 = 2 * I_WIN, C1 = C0 + 2 * I_WOUT, C2 = C1 + I_GU, C3 = C2 + I_DN, C4 = C3 + 8 * I_GU, C5 = C4 + 8 * I_DN, C6 = C5 + 2 * I_PG, C7 = C6 + 2 * I_PP;
;     unsigned char* ws = P.ws;
;     for (int it = (PART == 0 ? 0 : I_WIN) + gw; it < (PART == 0 ? I_WIN : C7); it += NGW) {
;     ...
;     const int gt = F.bid * NTHR + F.tid, NGT = F.G * NTHR;
;     float* WGT = (float*)(ws + WS_WGT); float* WRT = (float*)(ws + WS_WRT);
;     for (int e = gt; e < 2 * 16 * D; e += NGT) { const int l = e / (16 * D), j = (e / D) % 16, k = e % D; const int col = j < 8 ? 3072 + j : 7176 + (j - 8);
;         WGT[e] = P.in[I_W_IN][((size_t)l * D + k) * NIN + col]; }
;     for (int e = gt; e < NEXP * D; e += NGT) { const int j = e / D, k = e % D; WRT[e] = P.in[I_ROUTER][(size_t)k * NEXP + j]; }
.LBB0_11:
	s_or_b64 exec, exec, s[0:1]
	s_load_dwordx16 s[4:19], s[62:63], 0x40
	s_lshr_b32 s86, s87, 6
	s_cmp_lt_i32 s64, 1
	s_cselect_b64 s[0:1], -1, 0
	s_cmp_gt_i32 s65, 0
	s_waitcnt lgkmcnt(0)
	v_writelane_b32 v254, s4, 5
	s_nop 1
	v_writelane_b32 v254, s5, 6
	v_writelane_b32 v254, s6, 7
	v_writelane_b32 v254, s7, 8
	v_writelane_b32 v254, s8, 9
	v_writelane_b32 v254, s9, 10
	v_writelane_b32 v254, s10, 11
	v_writelane_b32 v254, s11, 12
	v_writelane_b32 v254, s12, 13
	v_writelane_b32 v254, s13, 14
	v_writelane_b32 v254, s14, 15
	v_writelane_b32 v254, s15, 16
	v_writelane_b32 v254, s16, 17
	v_writelane_b32 v254, s17, 18
	v_writelane_b32 v254, s18, 19
	v_writelane_b32 v254, s19, 20
	s_load_dwordx16 s[4:19], s[62:63], 0x80
	s_waitcnt lgkmcnt(0)
	v_writelane_b32 v254, s4, 21
	s_nop 1
	v_writelane_b32 v254, s5, 22
	v_writelane_b32 v254, s6, 23
	v_writelane_b32 v254, s7, 24
	v_writelane_b32 v254, s8, 25
	v_writelane_b32 v254, s9, 26
	v_writelane_b32 v254, s10, 27
	v_writelane_b32 v254, s11, 28
	v_writelane_b32 v254, s12, 29
	v_writelane_b32 v254, s13, 30
	v_writelane_b32 v254, s14, 31
	v_writelane_b32 v254, s15, 32
	v_writelane_b32 v254, s16, 33
	v_writelane_b32 v254, s17, 34
	v_writelane_b32 v254, s18, 35
	v_writelane_b32 v254, s19, 36
	s_cselect_b64 s[4:5], -1, 0
	s_and_b64 s[0:1], s[0:1], s[4:5]
	s_andn2_b64 vcc, exec, s[0:1]
	s_cbranch_vccnz .LBB0_75
	s_lshl_b32 s0, s2, 3
	v_mbcnt_lo_u32_b32 v0, -1, 0
	s_add_i32 s3, s86, s0
	v_mbcnt_hi_u32_b32 v2, -1, v0
	s_and_b32 s0, s87, 0xffffffc0
	s_lshl_b32 s1, s2, 9
	s_add_i32 s0, s0, s1
	v_add_u32_e32 v100, s0, v2
	s_mov_b32 s0, 0x10000
	v_cmp_gt_i32_e32 vcc, s0, v100
	s_and_saveexec_b64 s[4:5], vcc
	s_movk_i32 s6, 0x7040
	v_mov_b32_e32 v108, 0x1c00
	v_mov_b32_e32 v109, 0xc00
	v_mov_b32_e32 v105, 0
	v_mov_b64_e32 v[106:107], s[74:75]
	v_ashrrev_i32_e32 v104, 31, v100
	v_lshrrev_b32_e32 v111, 17, v104
	v_lshrrev_b32_e32 v104, 21, v104
	v_add_u32_e32 v104, v100, v104
	v_add_u32_e32 v111, v100, v111
	v_ashrrev_i32_e32 v104, 11, v104
	v_ashrrev_i32_e32 v112, 15, v111
	v_lshrrev_b32_e32 v111, 28, v104
	v_mul_i32_i24_e32 v114, 0x800, v104
	v_add_u32_e32 v111, v104, v111
	v_ashrrev_i32_e32 v113, 31, v112
	v_sub_u32_e32 v114, v100, v114
	v_and_b32_e32 v111, -16, v111
	v_lshlrev_b64 v[112:113], 11, v[112:113]
	v_ashrrev_i32_e32 v115, 31, v114
	v_sub_u32_e32 v104, v104, v111
	v_lshl_add_u64 v[112:113], v[112:113], 0, v[114:115]
	v_cmp_gt_i32_e32 vcc, 8, v104
	v_mad_u64_u32 v[114:115], s[0:1], v112, s6, v[106:107]
	s_nop 0
	v_cndmask_b32_e32 v111, v108, v109, vcc
	v_add_u32_e32 v104, v111, v104
	v_mad_i32_i24 v115, v113, s6, v115
	v_lshl_add_u64 v[112:113], v[104:105], 2, v[114:115]
	global_load_dword v101, v[112:113], off
	s_mov_b64 exec, s[4:5]
	s_load_dwordx2 s[0:1], s[62:63], 0xb0
	s_movk_i32 s6, 0x4000
	v_cmp_gt_i32_e32 vcc, s6, v100
	s_and_saveexec_b64 s[4:5], vcc
	v_ashrrev_i32_e32 v116, 31, v100
	v_lshrrev_b32_e32 v116, 21, v116
	v_add_u32_e32 v116, v100, v116
	v_ashrrev_i32_e32 v118, 11, v116
	v_mul_i32_i24_e32 v116, 0x800, v118
	v_sub_u32_e32 v120, v100, v116
	v_ashrrev_i32_e32 v121, 31, v120
	v_lshlrev_b64 v[120:121], 5, v[120:121]
	v_ashrrev_i32_e32 v119, 31, v118
	s_waitcnt lgkmcnt(0)
	v_lshl_add_u64 v[120:121], s[0:1], 0, v[120:121]
	v_lshl_add_u64 v[118:119], v[118:119], 2, v[120:121]
	global_load_dword v102, v[118:119], off
	s_mov_b64 exec, s[4:5]
	s_cmpk_gt_i32 s3, 0xdff
	s_cbranch_scc1 .LBB0_15
	v_ashrrev_i32_e32 v3, 4, v2
	s_mul_i32 s0, s86, 0x2400
	v_bfe_u32 v6, v2, 2, 2
	v_lshlrev_b32_e32 v5, 3, v3
	s_add_i32 s0, s0, 0
	v_and_b32_e32 v4, 15, v2
	s_movk_i32 s1, 0x90
	v_or_b32_e32 v6, v5, v6
	v_lshlrev_b32_e32 v7, 3, v2
	v_lshl_add_u32 v14, v4, 3, s0
	v_mul_lo_u32 v15, v3, s1
	v_mul_lo_u32 v6, v6, s1
	v_and_b32_e32 v7, 24, v7
	s_add_u32 s4, s54, 0x800000
	v_lshlrev_b32_e32 v0, 2, v4
	v_add3_u32 v6, v7, s0, v6
	v_add_u32_e32 v14, v14, v15
	s_addc_u32 s5, s55, 0
	v_mov_b32_e32 v1, 0
	v_add_u32_e32 v7, 0x1200, v6
	v_add_u32_e32 v8, 32, v6
	v_add_u32_e32 v9, 0x1220, v6
	v_add_u32_e32 v10, 64, v6
	v_add_u32_e32 v11, 0x1240, v6
	v_add_u32_e32 v12, 0x60, v6
	v_add_u32_e32 v13, 0x1260, v6
	v_lshlrev_b32_e32 v0, 2, v0
	s_movk_i32 s6, 0x7040
	v_add_u32_e32 v15, 0x800, v14
	v_add_u32_e32 v16, 0x1000, v14
	v_add_u32_e32 v17, 0x1400, v14
	v_add_u32_e32 v18, 0x1800, v14
	v_add_u32_e32 v19, 0x1c00, v14

; template <int PART> DI void prologue_phase(const Params& P, const Frame& F) {
;     ...
;     for (int e = gt; e < 2 * 16 * D; e += NGT) { const int l = e / (16 * D), j = (e / D) % 16, k = e % D; const int col = j < 8 ? 3072 + j : 7176 + (j - 8);
;         WGT[e] = P.in[I_W_IN][((size_t)l * D + k) * NIN + col]; }
.LBB0_17:
	v_ashrrev_i32_e32 v4, 31, v10
	v_lshrrev_b32_e32 v11, 17, v4
	v_lshrrev_b32_e32 v4, 21, v4
	v_add_u32_e32 v4, v10, v4
	v_add_u32_e32 v11, v10, v11
	v_ashrrev_i32_e32 v4, 11, v4
	v_ashrrev_i32_e32 v12, 15, v11
	v_lshrrev_b32_e32 v11, 28, v4
	v_mul_i32_i24_e32 v14, 0x800, v4
	v_add_u32_e32 v11, v4, v11
	v_ashrrev_i32_e32 v13, 31, v12
	v_sub_u32_e32 v14, v10, v14
	v_and_b32_e32 v11, -16, v11
	v_lshlrev_b64 v[12:13], 11, v[12:13]
	v_ashrrev_i32_e32 v15, 31, v14
	v_sub_u32_e32 v4, v4, v11
	v_lshl_add_u64 v[12:13], v[12:13], 0, v[14:15]
	v_cmp_gt_i32_e32 vcc, 8, v4
	v_mad_u64_u32 v[14:15], s[10:11], v12, s3, v[6:7]
	s_nop 0
	v_cndmask_b32_e32 v11, v8, v9, vcc
	v_add_u32_e32 v4, v11, v4
	v_mad_i32_i24 v15, v13, s3, v15
	v_lshl_add_u64 v[12:13], v[4:5], 2, v[14:15]
	v_mov_b32_e32 v4, v101
	v_add_u32_e32 v11, 0x20000, v10
	v_cmp_lt_i32_e32 vcc, s8, v10
	s_or_b64 s[4:5], vcc, s[4:5]
	v_mov_b32_e32 v10, v11
	s_waitcnt vmcnt(0)
	global_store_dword v[2:3], v4, off
	v_lshl_add_u64 v[2:3], v[2:3], 0, s[6:7]
	s_andn2_b64 exec, exec, s[4:5]
	s_cbranch_execnz .LBB0_17

; template <int PART> DI void prologue_phase(const Params& P, const Frame& F) {
;     ...
;     for (int e = gt; e < NEXP * D; e += NGT) { const int j = e / D, k = e % D; WRT[e] = P.in[I_ROUTER][(size_t)k * NEXP + j]; }
.LBB0_20:
	v_ashrrev_i32_e32 v1, 31, v0
	v_lshrrev_b32_e32 v1, 21, v1
	v_add_u32_e32 v1, v0, v1
	v_ashrrev_i32_e32 v4, 11, v1
	v_mul_i32_i24_e32 v1, 0x800, v4
	v_sub_u32_e32 v6, v0, v1
	v_ashrrev_i32_e32 v7, 31, v6
	v_lshlrev_b64 v[6:7], 5, v[6:7]
	v_ashrrev_i32_e32 v5, 31, v4
	s_waitcnt lgkmcnt(0)
	v_lshl_add_u64 v[6:7], s[20:21], 0, v[6:7]
	v_lshl_add_u64 v[4:5], v[4:5], 2, v[6:7]
	v_mov_b32_e32 v1, v102
	v_add_u32_e32 v4, 0x20000, v0
	v_cmp_lt_i32_e32 vcc, s3, v0
	s_or_b64 s[4:5], vcc, s[4:5]
	v_mov_b32_e32 v0, v4
	s_waitcnt vmcnt(0)
	global_store_dword v[2:3], v1, off
	v_lshl_add_u64 v[2:3], v[2:3], 0, s[6:7]
	s_andn2_b64 exec, exec, s[4:5]
	s_cbranch_execnz .LBB0_20

.LBB0_66:
	s_cmp_lt_u32 s3, 0x40001
	s_mov_b64 s[18:19], 0
	s_cselect_b64 s[20:21], -1, 0
	s_mov_b64 s[22:23], -1
	s_and_b64 vcc, exec, s[20:21]
	s_cbranch_vccnz .LBB0_63
	s_branch .LBB0_60
	s_nop 0
	s_nop 0
	s_nop 0
	s_nop 0
	s_nop 0
	s_nop 0
	s_nop 0
	s_nop 0
	s_nop 0
	s_nop 0
	s_nop 0
	s_nop 0
	s_nop 0
	s_nop 0
	s_nop 0
	s_nop 0
	s_nop 0
	s_nop 0
	s_nop 0
	s_nop 0
	s_nop 0
	s_nop 0
	s_nop 0
	s_nop 0
	s_nop 0
	s_nop 0
	s_nop 0
	s_nop 0
	s_nop 0
	s_nop 0
	s_nop 0
	s_nop 0
	s_nop 0
	s_nop 0
	s_nop 0
	s_nop 0
	s_nop 0
	s_nop 0
	s_nop 0
	s_nop 0
	s_nop 0
	s_nop 0
	s_nop 0
	s_nop 0
	s_nop 0
	s_nop 0
	s_nop 0
	s_nop 0
	s_nop 0
	s_nop 0
	s_nop 0
	s_nop 0
	s_nop 0
	s_nop 0
	s_nop 0
	s_nop 0
	s_nop 0

; DI float wave_sum(float v) { v += shx<1>(v); v += shx<2>(v); v += shx<4>(v); v += shx<8>(v); v += shx<16>(v); v += shx<32>(v); return v; }
; #define PH_BEGIN(k, kind) if (lo <= (k) && (k) < hi) { PH_SETUP()
; template <int L> DI void layer_phases(const Params& P, Frame& F, const XcdBarrier& bar, int lo, int hi) {
;     ...
;         PH_BEGIN(pb + 4, 4) {
;             if (F.bid < 32) dn2_block(P, F, L, F.bid); else ml2_scan(P, (F.bid - 32) * NTHR + F.tid, (F.G - 32) * NTHR);
;             const float li = (L == 0) ? 0.2f : 0.35550906759f;
;             const float d1 = wave_sum(P.in[I_LQ1][L * 64 + F.lane] * P.in[I_LK1][L * 64 + F.lane]), d2 = wave_sum(P.in[I_LQ2][L * 64 + F.lane] * P.in[I_LK2][L * 64 + F.lane]);
.LBB0_1026:
	s_cmp_gt_i32 s64, 5
	s_cselect_b64 s[0:1], -1, 0
	s_cmp_lt_i32 s65, 6
	s_cselect_b64 s[4:5], -1, 0
	s_or_b64 s[0:1], s[0:1], s[4:5]
	s_and_b64 vcc, exec, s[0:1]
	s_cbranch_vccnz .LBB0_1124
	v_mbcnt_lo_u32_b32 v0, -1, 0
	v_mbcnt_hi_u32_b32 v193, -1, v0
	v_mov_b32_e32 v136, v193
	v_lshlrev_b32_e32 v253, 2, v136
	v_readlane_b32 s0, v254, 7
	v_readlane_b32 s1, v254, 8
	v_readlane_b32 s4, v254, 9
	v_readlane_b32 s5, v254, 10
	s_nop 4
	global_load_dword v248, v253, s[0:1]
	global_load_dword v249, v253, s[4:5]
	v_readlane_b32 s0, v254, 11
	v_readlane_b32 s1, v254, 12
	v_readlane_b32 s4, v254, 13
	v_readlane_b32 s5, v254, 14
	s_nop 4
	global_load_dword v250, v253, s[0:1]
	global_load_dword v251, v253, s[4:5]
	s_and_b32 s0, s87, 0xffffffc0
	s_cmp_gt_i32 s2, 31
	v_add_u32_e32 v138, s0, v136
	s_mov_b64 s[0:1], -1
	s_cbranch_scc0 .LBB0_1034
	s_lshl_b32 s0, s2, 9
	s_addk_i32 s0, 0xc000
	s_waitcnt vmcnt(12)
	v_add_u32_e32 v46, s0, v138
	s_mov_b32 s0, 0x20400
	v_cmp_gt_i32_e32 vcc, s0, v46
	s_and_saveexec_b64 s[0:1], vcc
	s_cbranch_execz .LBB0_1033
	s_mov_b64 s[4:5], 0
	s_mov_b64 s[6:7], 0x500000
	s_waitcnt lgkmcnt(0)
	s_mov_b64 s[8:9], 0x501000
	s_mov_b32 s3, 0x5f009000
	s_mov_b32 s14, 0x5f012000
	s_mov_b32 s15, 0x5f01b000
	s_mov_b32 s16, 0x5f024000
	s_mov_b32 s17, 0x5f02d000
	s_mov_b32 s18, 0x5f036000
	s_mov_b32 s19, 0x5f03f000
	s_mov_b64 s[10:11], 0x48000
	s_mov_b64 s[12:13], 0x81000
	s_movk_i32 s20, 0x43ff

; DI float wave_sum(float v) { v += shx<1>(v); v += shx<2>(v); v += shx<4>(v); v += shx<8>(v); v += shx<16>(v); v += shx<32>(v); return v; }
; template <int L> DI void layer_phases(const Params& P, Frame& F, const XcdBarrier& bar, int lo, int hi) {
;     ...
;             const float li = (L == 0) ? 0.2f : 0.35550906759f;
;             const float d1 = wave_sum(P.in[I_LQ1][L * 64 + F.lane] * P.in[I_LK1][L * 64 + F.lane]), d2 = wave_sum(P.in[I_LQ2][L * 64 + F.lane] * P.in[I_LK2][L * 64 + F.lane]);
;             const float lam = __expf(d1) - __expf(d2) + li;
.LBB0_1045:
	v_ashrrev_i32_e32 v137, 31, v136
	s_waitcnt lgkmcnt(0)
	v_readlane_b32 s4, v254, 5
	v_lshlrev_b64 v[0:1], 2, v[136:137]
	v_readlane_b32 s6, v254, 7
	v_readlane_b32 s7, v254, 8
	v_readlane_b32 s8, v254, 9
	v_readlane_b32 s9, v254, 10
	v_lshl_add_u64 v[2:3], s[6:7], 0, v[0:1]
	v_readlane_b32 s10, v254, 11
	v_readlane_b32 s11, v254, 12
	v_readlane_b32 s12, v254, 13
	v_readlane_b32 s13, v254, 14
	v_mov_b32_e32 v4, v248
	v_lshl_add_u64 v[2:3], s[8:9], 0, v[0:1]
	v_mov_b32_e32 v5, v249
	v_lshl_add_u64 v[2:3], s[10:11], 0, v[0:1]
	v_lshl_add_u64 v[0:1], s[12:13], 0, v[0:1]
	v_mov_b32_e32 v2, v250
	v_xor_b32_e32 v3, 32, v193
	v_mov_b32_e32 v1, v251
	v_and_b32_e32 v0, 64, v193
	v_add_u32_e32 v12, 64, v0
	v_ashrrev_i32_e32 v6, 4, v136
	v_cmp_lt_i32_e32 vcc, v3, v12
	v_add_u32_e32 v8, 0x200, v138
	v_bfe_u32 v9, v136, 3, 1
	s_movk_i32 s6, 0x2400
	v_bfe_u32 v11, v136, 2, 2
	v_lshlrev_b32_e32 v130, 2, v6
	v_cndmask_b32_e32 v3, v193, v3, vcc
	v_ashrrev_i32_e32 v128, 4, v8
	v_mul_u32_u24_e32 v182, 0x2400, v9
	v_mad_u32_u24 v8, v9, s6, 0
	v_or_b32_e32 v9, v130, v11
	v_lshlrev_b32_e32 v190, 2, v3
	v_lshlrev_b32_e32 v7, 3, v136
	v_ashrrev_i32_e32 v114, 4, v138
	s_movk_i32 s7, 0x90
	s_movk_i32 s8, 0x110
	v_and_b32_e32 v0, 24, v7
	v_mul_lo_u32 v183, v114, s7
	v_mul_lo_u32 v188, v128, s7
	s_add_u32 s0, s54, 0x2000
	s_addc_u32 s1, s55, 0
	v_lshlrev_b32_e32 v10, 4, v136
	s_add_u32 s58, s54, 0x41600000
	v_and_b32_e32 v127, 15, v136
	v_lshlrev_b32_e32 v124, 3, v6
	v_and_b32_e32 v184, 0x70, v10
	v_add_u32_e32 v6, v8, v183
	s_addc_u32 s59, s55, 0
	s_lshl_b32 s64, s86, 4
	v_mul_lo_u32 v185, v114, s8
	v_mul_lo_u32 v189, v128, s8
	v_sub_u32_e32 v10, v130, v127
	v_readlane_b32 s5, v254, 6
	v_readlane_b32 s14, v254, 15
	v_readlane_b32 s15, v254, 16
	v_and_b32_e32 v126, 0x78, v7
	v_lshlrev_b32_e32 v186, 4, v127
	v_add_u32_e32 v7, 0, v185
	v_ashrrev_i32_e32 v131, 31, v130
	s_mov_b32 s39, 0
	v_cmp_eq_u32_e64 s[4:5], 0, v138
	v_mov_b32_e32 v113, 0
	v_and_b32_e32 v161, -16, v136
	s_movk_i32 s3, 0x3800
	s_mov_b32 s56, 0x3e38aa3b
	s_movk_i32 s33, 0x2000
	s_mov_b32 s57, 0xff800000
	v_mov_b32_e32 v179, 0x358637bd
	v_mov_b32_e32 v180, 0x42800000
	v_mov_b32_e32 v181, 0x3fb8aa3b
	v_mov_b32_e32 v116, 2.0
	v_mov_b32_e32 v117, 0x40400000
	v_mov_b32_e32 v118, 0x41800000
	v_mov_b32_e32 v119, 0x41880000
	v_mov_b32_e32 v120, 0x41900000
	v_mov_b32_e32 v121, 0x41980000
	v_mov_b32_e32 v122, 0x42000000
	v_mov_b32_e32 v123, 0x42040000
	v_ashrrev_i32_e32 v115, 31, v114
	v_mul_u32_u24_e32 v187, 0x90, v127
	v_ashrrev_i32_e32 v125, 31, v124
	v_ashrrev_i32_e32 v129, 31, v128
	v_lshl_add_u64 v[134:135], v[130:131], 2, s[14:15]
	s_add_i32 s65, 0, 0x22060
	v_add_u32_e32 v191, v7, v186
	v_mov_b32_e32 v136, 0x42080000
	v_mov_b32_e32 v137, 0x420c0000
	v_mov_b32_e32 v138, 0x42400000
	v_mov_b32_e32 v139, 0x42440000
	v_mov_b32_e32 v140, 0x42480000
	v_mov_b32_e32 v141, 0x424c0000
	s_waitcnt vmcnt(2)
	v_mul_f32_e32 v3, v4, v5
	v_mov_b32_e32 v198, 0xff800000
	v_readlane_b32 s16, v254, 17
	v_mov_b32_dpp v3, v3 quad_perm:[1,0,3,2] row_mask:0xf bank_mask:0xf bound_ctrl:1
	v_fmac_f32_e32 v3, v4, v5
	s_waitcnt vmcnt(0)
	v_mul_f32_e32 v11, v2, v1
	v_add_u32_e32 v5, v8, v188
	v_add_u32_e32 v8, 0, v189
	v_mov_b32_dpp v11, v11 quad_perm:[1,0,3,2] row_mask:0xf bank_mask:0xf bound_ctrl:1
	v_fmac_f32_e32 v11, v2, v1
	v_add_f32_dpp v1, v3, v3 quad_perm:[2,3,0,1] row_mask:0xf bank_mask:0xf bound_ctrl:1
	ds_swizzle_b32 v3, v1 offset:swizzle(SWAP,4)
	v_add_f32_dpp v2, v11, v11 quad_perm:[2,3,0,1] row_mask:0xf bank_mask:0xf bound_ctrl:1
	ds_swizzle_b32 v4, v2 offset:swizzle(SWAP,4)
	v_add_u32_e32 v193, v5, v184
	v_add_u32_e32 v194, v8, v186
	s_waitcnt lgkmcnt(1)
	v_add_f32_e32 v1, v1, v3
	ds_swizzle_b32 v3, v1 offset:swizzle(SWAP,8)
	s_waitcnt lgkmcnt(1)
	v_add_f32_e32 v2, v2, v4
	ds_swizzle_b32 v4, v2 offset:swizzle(SWAP,8)
	v_mad_u64_u32 v[132:133], s[6:7], v9, s8, v[0:1]
	s_waitcnt lgkmcnt(1)
	v_add_f32_e32 v0, v1, v3
	v_add_u32_e32 v133, v6, v184
	s_waitcnt lgkmcnt(0)
	v_add_f32_e32 v1, v2, v4
	ds_swizzle_b32 v2, v0 offset:swizzle(SWAP,16)
	ds_swizzle_b32 v3, v1 offset:swizzle(SWAP,16)
	v_or_b32_e32 v6, s64, v127
	v_subrev_u32_e32 v4, s64, v10
	v_add_u32_e32 v195, 64, v4
	s_waitcnt lgkmcnt(1)
	v_add_f32_e32 v0, v0, v2
	s_waitcnt lgkmcnt(0)
	v_add_f32_e32 v1, v1, v3
	ds_bpermute_b32 v2, v190, v0
	ds_bpermute_b32 v3, v190, v1
	v_readlane_b32 s17, v254, 18
	v_readlane_b32 s18, v254, 19
	v_readlane_b32 s19, v254, 20
	s_waitcnt lgkmcnt(1)
	v_add_f32_e32 v0, v0, v2
	s_waitcnt lgkmcnt(0)
	v_add_f32_e32 v1, v1, v3
	v_mul_f32_e32 v0, 0x3fb8aa3b, v0
	v_mul_f32_e32 v1, 0x3fb8aa3b, v1
	v_exp_f32_e32 v0, v0
	v_exp_f32_e32 v1, v1
	v_sub_u32_e32 v2, v6, v130
	v_subrev_u32_e32 v196, 64, v2
	v_sub_f32_e32 v0, v0, v1
	v_add_f32_e32 v197, 0x3e4ccccd, v0
	s_mov_b64 s[6:7], exec
	s_and_b64 exec, exec, s[4:5]
	v_mov_b32_e32 v252, 1
	global_atomic_add v252, v113, v252, s[0:1] sc0
	s_mov_b64 exec, s[6:7]
	s_branch .LBB0_1048

.LBB0_1115:
	s_cmp_lt_u32 s3, 0x40001
	s_mov_b64 s[18:19], 0
	s_cselect_b64 s[20:21], -1, 0
	s_mov_b64 s[22:23], -1
	s_and_b64 vcc, exec, s[20:21]
	s_cbranch_vccnz .LBB0_1112
	s_branch .LBB0_1109
	s_nop 0
	s_nop 0
	s_nop 0
	s_nop 0
	s_nop 0
	s_nop 0
	s_nop 0
	s_nop 0
	s_nop 0
	s_nop 0
	s_nop 0
	s_nop 0
	s_nop 0
	s_nop 0
	s_nop 0
	s_nop 0
	s_nop 0
	s_nop 0
	s_nop 0
	s_nop 0
	s_nop 0
	s_nop 0
	s_nop 0
	s_nop 0
	s_nop 0
	s_nop 0
	s_nop 0
	s_nop 0
	s_nop 0
	s_nop 0
	s_nop 0
	s_nop 0
	s_nop 0
	s_nop 0
	s_nop 0
	s_nop 0
	s_nop 0
	s_nop 0
	s_nop 0
	s_nop 0
	s_nop 0
	s_nop 0
	s_nop 0
	s_nop 0
	s_nop 0

; DI float wave_sum(float v) { v += shx<1>(v); v += shx<2>(v); v += shx<4>(v); v += shx<8>(v); v += shx<16>(v); v += shx<32>(v); return v; }
; #define PH_BEGIN(k, kind) if (lo <= (k) && (k) < hi) { PH_SETUP()
; template <int L> DI void layer_phases(const Params& P, Frame& F, const XcdBarrier& bar, int lo, int hi) {
;     ...
;         PH_BEGIN(pb + 4, 4) {
;             if (F.bid < 32) dn2_block(P, F, L, F.bid); else ml2_scan(P, (F.bid - 32) * NTHR + F.tid, (F.G - 32) * NTHR);
;             const float li = (L == 0) ? 0.2f : 0.35550906759f;
;             const float d1 = wave_sum(P.in[I_LQ1][L * 64 + F.lane] * P.in[I_LK1][L * 64 + F.lane]), d2 = wave_sum(P.in[I_LQ2][L * 64 + F.lane] * P.in[I_LK2][L * 64 + F.lane]);
.LBB0_2591:
	s_cmp_gt_i32 s64, 18
	s_cselect_b64 s[0:1], -1, 0
	s_cmp_lt_i32 s65, 19
	s_cselect_b64 s[4:5], -1, 0
	s_or_b64 s[0:1], s[0:1], s[4:5]
	s_and_b64 vcc, exec, s[0:1]
	s_cbranch_vccnz .LBB0_2689
	v_mbcnt_lo_u32_b32 v0, -1, 0
	v_mbcnt_hi_u32_b32 v154, -1, v0
	v_mov_b32_e32 v112, v154
	v_lshlrev_b32_e32 v253, 2, v112
	v_readlane_b32 s0, v254, 7
	v_readlane_b32 s1, v254, 8
	v_readlane_b32 s4, v254, 9
	v_readlane_b32 s5, v254, 10
	s_nop 4
	global_load_dword v248, v253, s[0:1] offset:256
	global_load_dword v249, v253, s[4:5] offset:256
	v_readlane_b32 s0, v254, 11
	v_readlane_b32 s1, v254, 12
	v_readlane_b32 s4, v254, 13
	v_readlane_b32 s5, v254, 14
	s_nop 4
	global_load_dword v250, v253, s[0:1] offset:256
	global_load_dword v251, v253, s[4:5] offset:256
	s_and_b32 s0, s87, 0xffffffc0
	s_cmp_gt_i32 s2, 31
	v_add_u32_e32 v114, s0, v112
	s_mov_b64 s[0:1], -1
	s_cbranch_scc0 .LBB0_2599
	s_lshl_b32 s0, s2, 9
	s_addk_i32 s0, 0xc000
	v_add_u32_e32 v12, s0, v114
	s_mov_b32 s0, 0x20400
	v_cmp_gt_i32_e32 vcc, s0, v12
	s_and_saveexec_b64 s[0:1], vcc
	s_cbranch_execz .LBB0_2598
	s_mov_b64 s[4:5], 0
	s_mov_b32 s3, 0xfe03f81
	s_mov_b32 s14, 0x9000
	s_mov_b32 s15, 0x10200
	s_mov_b64 s[6:7], 0x500000
	s_mov_b64 s[8:9], 0x501000
	s_mov_b32 s16, 0x5f009000
	s_mov_b32 s17, 0x5f012000
	s_mov_b32 s18, 0x5f01b000
	s_mov_b32 s19, 0x5f024000
	s_mov_b32 s20, 0x5f02d000
	s_mov_b32 s21, 0x5f036000
	s_mov_b32 s22, 0x5f03f000
	s_mov_b64 s[10:11], 0x48000
	s_mov_b64 s[12:13], 0x81000
	s_movk_i32 s23, 0x43ff

; DI float wave_sum(float v) { v += shx<1>(v); v += shx<2>(v); v += shx<4>(v); v += shx<8>(v); v += shx<16>(v); v += shx<32>(v); return v; }
; template <int L> DI void layer_phases(const Params& P, Frame& F, const XcdBarrier& bar, int lo, int hi) {
;     ...
;             const float li = (L == 0) ? 0.2f : 0.35550906759f;
;             const float d1 = wave_sum(P.in[I_LQ1][L * 64 + F.lane] * P.in[I_LK1][L * 64 + F.lane]), d2 = wave_sum(P.in[I_LQ2][L * 64 + F.lane] * P.in[I_LK2][L * 64 + F.lane]);
;             const float lam = __expf(d1) - __expf(d2) + li;
.LBB0_2610:
	v_ashrrev_i32_e32 v113, 31, v112
	v_readlane_b32 s4, v254, 5
	v_lshlrev_b64 v[0:1], 2, v[112:113]
	v_readlane_b32 s6, v254, 7
	v_readlane_b32 s7, v254, 8
	v_readlane_b32 s8, v254, 9
	v_readlane_b32 s9, v254, 10
	v_lshl_add_u64 v[2:3], s[6:7], 0, v[0:1]
	v_readlane_b32 s10, v254, 11
	v_readlane_b32 s11, v254, 12
	v_readlane_b32 s12, v254, 13
	v_readlane_b32 s13, v254, 14
	v_mov_b32_e32 v4, v248
	v_lshl_add_u64 v[2:3], s[8:9], 0, v[0:1]
	v_mov_b32_e32 v5, v249
	v_lshl_add_u64 v[2:3], s[10:11], 0, v[0:1]
	v_lshl_add_u64 v[0:1], s[12:13], 0, v[0:1]
	v_mov_b32_e32 v2, v250
	v_xor_b32_e32 v3, 32, v154
	v_mov_b32_e32 v1, v251
	v_and_b32_e32 v0, 64, v154
	v_add_u32_e32 v12, 64, v0
	v_ashrrev_i32_e32 v6, 4, v112
	v_cmp_lt_i32_e32 vcc, v3, v12
	v_add_u32_e32 v8, 0x200, v114
	v_bfe_u32 v9, v112, 3, 1
	s_movk_i32 s6, 0x2400
	v_bfe_u32 v11, v112, 2, 2
	v_lshlrev_b32_e32 v106, 2, v6
	v_cndmask_b32_e32 v3, v154, v3, vcc
	v_ashrrev_i32_e32 v104, 4, v8
	v_mul_u32_u24_e32 v182, 0x2400, v9
	v_mad_u32_u24 v8, v9, s6, 0
	v_or_b32_e32 v9, v106, v11
	v_lshlrev_b32_e32 v190, 2, v3
	v_lshlrev_b32_e32 v7, 3, v112
	v_ashrrev_i32_e32 v98, 4, v114
	s_movk_i32 s7, 0x90
	s_movk_i32 s8, 0x110
	v_and_b32_e32 v0, 24, v7
	v_mul_lo_u32 v183, v98, s7
	v_mul_lo_u32 v188, v104, s7
	s_add_u32 s0, s54, 0x2100
	s_addc_u32 s1, s55, 0
	v_lshlrev_b32_e32 v10, 4, v112
	s_add_u32 s56, s54, 0x41600000
	v_and_b32_e32 v103, 15, v112
	v_lshlrev_b32_e32 v100, 3, v6
	v_and_b32_e32 v184, 0x70, v10
	v_add_u32_e32 v6, v8, v183
	s_addc_u32 s57, s55, 0
	s_lshl_b32 s66, s86, 4
	v_mul_lo_u32 v185, v98, s8
	v_mul_lo_u32 v189, v104, s8
	v_sub_u32_e32 v10, v106, v103
	v_readlane_b32 s5, v254, 6
	v_readlane_b32 s14, v254, 15
	v_readlane_b32 s15, v254, 16
	v_and_b32_e32 v102, 0x78, v7
	v_lshlrev_b32_e32 v186, 4, v103
	v_add_u32_e32 v7, 0, v185
	v_ashrrev_i32_e32 v107, 31, v106
	s_mov_b32 s41, 0
	v_cmp_eq_u32_e64 s[4:5], 0, v114
	v_mov_b32_e32 v97, 0
	v_and_b32_e32 v145, -16, v112
	s_movk_i32 s3, 0x3ff
	s_movk_i32 s33, 0x3800
	s_mov_b64 s[42:43], 0x1800
	s_movk_i32 s47, 0x1000
	s_mov_b32 s62, 0x42fc0000
	s_mov_b32 s46, 0x3e38aa3b
	s_movk_i32 s63, 0x2000
	s_mov_b32 s64, 0xff800000
	v_mov_b32_e32 v163, 0x358637bd
	s_mov_b64 s[48:49], 0x61400400
	s_mov_b32 s65, 0x61400000
	v_mov_b32_e32 v180, 0x42800000
	v_mov_b32_e32 v181, 0x3fb8aa3b
	v_ashrrev_i32_e32 v99, 31, v98
	v_mul_u32_u24_e32 v187, 0x90, v103
	v_ashrrev_i32_e32 v101, 31, v100
	v_ashrrev_i32_e32 v105, 31, v104
	v_lshl_add_u64 v[110:111], v[106:107], 2, s[14:15]
	s_add_i32 s67, 0, 0x22060
	v_add_u32_e32 v191, v7, v186
	v_mov_b32_e32 v112, 2.0
	v_mov_b32_e32 v113, 0x40400000
	v_mov_b32_e32 v114, 0x41800000
	v_mov_b32_e32 v115, 0x41880000
	v_mov_b32_e32 v116, 0x41900000
	v_mov_b32_e32 v117, 0x41980000
	v_mov_b32_e32 v118, 0x42000000
	v_mov_b32_e32 v119, 0x42040000
	s_waitcnt vmcnt(2)
	v_mul_f32_e32 v3, v4, v5
	v_mov_b32_e32 v120, 0x42080000
	v_mov_b32_e32 v121, 0x420c0000
	v_mov_b32_dpp v3, v3 quad_perm:[1,0,3,2] row_mask:0xf bank_mask:0xf bound_ctrl:1
	v_fmac_f32_e32 v3, v4, v5
	s_waitcnt vmcnt(0)
	v_mul_f32_e32 v11, v2, v1
	v_add_u32_e32 v5, v8, v188
	v_add_u32_e32 v8, 0, v189
	v_mov_b32_dpp v11, v11 quad_perm:[1,0,3,2] row_mask:0xf bank_mask:0xf bound_ctrl:1
	v_fmac_f32_e32 v11, v2, v1
	v_add_f32_dpp v1, v3, v3 quad_perm:[2,3,0,1] row_mask:0xf bank_mask:0xf bound_ctrl:1
	ds_swizzle_b32 v3, v1 offset:swizzle(SWAP,4)
	v_add_f32_dpp v2, v11, v11 quad_perm:[2,3,0,1] row_mask:0xf bank_mask:0xf bound_ctrl:1
	ds_swizzle_b32 v4, v2 offset:swizzle(SWAP,4)
	v_add_u32_e32 v193, v5, v184
	v_add_u32_e32 v194, v8, v186
	s_waitcnt lgkmcnt(1)
	v_add_f32_e32 v1, v1, v3
	ds_swizzle_b32 v3, v1 offset:swizzle(SWAP,8)
	s_waitcnt lgkmcnt(1)
	v_add_f32_e32 v2, v2, v4
	ds_swizzle_b32 v4, v2 offset:swizzle(SWAP,8)
	v_mad_u64_u32 v[108:109], s[6:7], v9, s8, v[0:1]
	s_waitcnt lgkmcnt(1)
	v_add_f32_e32 v0, v1, v3
	v_add_u32_e32 v109, v6, v184
	s_waitcnt lgkmcnt(0)
	v_add_f32_e32 v1, v2, v4
	ds_swizzle_b32 v2, v0 offset:swizzle(SWAP,16)
	ds_swizzle_b32 v3, v1 offset:swizzle(SWAP,16)
	v_or_b32_e32 v6, s66, v103
	v_subrev_u32_e32 v4, s66, v10
	v_add_u32_e32 v195, 64, v4
	s_waitcnt lgkmcnt(1)
	v_add_f32_e32 v0, v0, v2
	s_waitcnt lgkmcnt(0)
	v_add_f32_e32 v1, v1, v3
	ds_bpermute_b32 v2, v190, v0
	ds_bpermute_b32 v3, v190, v1
	v_mov_b32_e32 v122, 0x42400000
	v_mov_b32_e32 v123, 0x42440000
	v_mov_b32_e32 v124, 0x42480000
	s_waitcnt lgkmcnt(1)
	v_add_f32_e32 v0, v0, v2
	s_waitcnt lgkmcnt(0)
	v_add_f32_e32 v1, v1, v3
	v_mul_f32_e32 v0, 0x3fb8aa3b, v0
	v_mul_f32_e32 v1, 0x3fb8aa3b, v1
	v_exp_f32_e32 v0, v0
	v_exp_f32_e32 v1, v1
	v_sub_u32_e32 v2, v6, v106
	v_subrev_u32_e32 v196, 64, v2
	v_mov_b32_e32 v125, 0x424c0000
	v_sub_f32_e32 v0, v0, v1
	v_add_f32_e32 v197, 0x3eb60549, v0
	v_mov_b32_e32 v198, 0xff800000
	v_readlane_b32 s16, v254, 17
	v_readlane_b32 s17, v254, 18
	v_readlane_b32 s18, v254, 19
	v_readlane_b32 s19, v254, 20
	s_mov_b64 s[6:7], exec
	s_and_b64 exec, exec, s[4:5]
	v_mov_b32_e32 v252, 1
	global_atomic_add v252, v97, v252, s[0:1] sc0
	s_mov_b64 exec, s[6:7]
	s_branch .LBB0_2613
